# baseline (speedup 1.0000x reference)
.LBB1_12:
	s_mov_b32 s0, s44
	s_add_i32 s44, s44, 1
	s_cmp_ge_u32 s44, s42
	s_cselect_b64 s[22:23], -1, 0
	s_cmp_lt_u32 s44, s42
	s_cselect_b32 s2, s44, s0
	s_waitcnt vmcnt(0)
	s_lshl_b32 s0, s2, 4
	s_mov_b32 s1, s17
	s_mov_b32 m0, s43
	ds_read_b128 v[76:79], v119 offset:32768
	ds_read_b128 v[80:83], v119 offset:36864
	ds_read_b128 v[84:87], v120 offset:32768
	ds_read_b128 v[88:91], v120 offset:36864
	ds_read_b128 v[92:95], v121
	ds_read_b128 v[96:99], v121 offset:4096
	ds_read_b128 v[128:131], v122
	ds_read_b128 v[132:135], v122 offset:4096
	ds_read_b128 v[72:75], v123
	s_waitcnt lgkmcnt(0)
	v_lshl_add_u64 v[70:71], s[0:1], 2, v[2:3]
	global_load_lds_dword v[70:71], off
	ds_read_b128 v[156:159], v115
	ds_read_b128 v[160:163], v115 offset:1024
	ds_read_b128 v[164:167], v115 offset:2048
	v_cvt_pk_bf16_f32 v136, v76, v77
	v_cvt_pk_bf16_f32 v137, v78, v79
	v_cvt_pk_bf16_f32 v138, v84, v85
	v_cvt_pk_bf16_f32 v139, v86, v87
	v_cvt_pk_bf16_f32 v140, v92, v93
	v_cvt_pk_bf16_f32 v141, v94, v95
	v_cvt_pk_bf16_f32 v142, v128, v129
	v_cvt_pk_bf16_f32 v143, v130, v131
	v_cvt_pk_bf16_f32 v144, v80, v81
	v_cvt_pk_bf16_f32 v145, v82, v83
	v_cvt_pk_bf16_f32 v146, v88, v89
	v_cvt_pk_bf16_f32 v147, v90, v91
	v_cvt_pk_bf16_f32 v128, v96, v97
	v_cvt_pk_bf16_f32 v129, v98, v99
	v_cvt_pk_bf16_f32 v130, v132, v133
	v_cvt_pk_bf16_f32 v131, v134, v135
	s_lshl_b32 s0, s2, 13
	s_cmp_lt_u32 s44, s42
	s_cselect_b32 s0, s0, 0x1e848000
	s_mov_b32 s61, s0
	s_add_i32 s63, s44, 1
	s_cmp_eq_u32 s63, s42
	s_cselect_b32 s63, 1, 0
	s_mov_b32 m0, s47
	s_nop 0
	buffer_load_dwordx4 v113, s[12:15], s61 offen nt lds
	s_cmp_eq_u32 s63, 0
	s_cbranch_scc1 .Lmain_noburst
	s_or_b32 s62, s61, 0x800
	s_mov_b32 m0, s48
	s_nop 0
	buffer_load_dwordx4 v113, s[12:15], s62 offen nt lds
	s_or_b32 s62, s61, 0x1000
	s_mov_b32 m0, s49
	s_nop 0
	buffer_load_dwordx4 v113, s[12:15], s62 offen nt lds
	s_or_b32 s62, s61, 0x1800
	s_mov_b32 m0, s50
	s_nop 0
	buffer_load_dwordx4 v113, s[12:15], s62 offen nt lds
	s_or_b32 s62, s61, 0x100
	s_mov_b32 m0, s51
	s_nop 0
	buffer_load_dwordx4 v113, s[12:15], s62 offen nt lds
	s_or_b32 s62, s61, 0x900
	s_mov_b32 m0, s52
	s_nop 0
	buffer_load_dwordx4 v113, s[12:15], s62 offen nt lds
	s_or_b32 s62, s61, 0x1100
	s_mov_b32 m0, s53
	s_nop 0
	buffer_load_dwordx4 v113, s[12:15], s62 offen nt lds
	s_or_b32 s62, s61, 0x1900
	s_mov_b32 m0, s54
	s_nop 0
	buffer_load_dwordx4 v113, s[12:15], s62 offen nt lds
.Lmain_noburst:
	ds_read_b128 v[132:135], v115 offset:3072
	s_waitcnt lgkmcnt(3)
	v_mfma_f32_16x16x32_bf16 v[148:151], v[136:139], v[156:159], v[36:39]
	ds_read_b128 v[156:159], v115 offset:4096
	s_waitcnt lgkmcnt(3)
	v_mfma_f32_16x16x32_bf16 v[152:155], v[136:139], v[160:163], v[40:43]
	ds_read_b128 v[160:163], v115 offset:5120
	s_waitcnt lgkmcnt(3)
	v_mfma_f32_16x16x32_bf16 v[96:99], v[136:139], v[164:167], v[44:47]
	ds_read_b128 v[164:167], v115 offset:6144
	s_waitcnt lgkmcnt(3)
	v_mfma_f32_16x16x32_bf16 v[92:95], v[136:139], v[132:135], v[48:51]
	ds_read_b128 v[132:135], v115 offset:7168
	s_waitcnt lgkmcnt(3)
	v_mfma_f32_16x16x32_bf16 v[88:91], v[136:139], v[156:159], v[52:55]
	ds_read_b128 v[156:159], v115 offset:8192
	s_waitcnt lgkmcnt(3)
	v_mfma_f32_16x16x32_bf16 v[84:87], v[136:139], v[160:163], v[56:59]
	ds_read_b128 v[160:163], v115 offset:9216
	s_waitcnt lgkmcnt(3)
	v_mfma_f32_16x16x32_bf16 v[80:83], v[136:139], v[164:167], v[60:63]
	ds_read_b128 v[164:167], v115 offset:10240
	s_waitcnt lgkmcnt(3)
	v_mfma_f32_16x16x32_bf16 v[76:79], v[136:139], v[132:135], v[64:67]
	ds_read_b128 v[132:135], v115 offset:11264
	s_waitcnt lgkmcnt(3)
	v_mfma_f32_16x16x32_bf16 v[148:151], v[140:143], v[156:159], v[148:151]
	ds_read_b128 v[156:159], v115 offset:12288
	s_waitcnt lgkmcnt(3)
	v_mfma_f32_16x16x32_bf16 v[152:155], v[140:143], v[160:163], v[152:155]
	ds_read_b128 v[160:163], v115 offset:13312
	s_waitcnt lgkmcnt(3)
	v_mfma_f32_16x16x32_bf16 v[96:99], v[140:143], v[164:167], v[96:99]
	ds_read_b128 v[164:167], v115 offset:14336
	s_waitcnt lgkmcnt(3)
	v_mfma_f32_16x16x32_bf16 v[92:95], v[140:143], v[132:135], v[92:95]
	ds_read_b128 v[132:135], v115 offset:15360
	s_waitcnt lgkmcnt(3)
	v_mfma_f32_16x16x32_bf16 v[88:91], v[140:143], v[156:159], v[88:91]
	ds_read_b128 v[156:159], v115 offset:16384
	s_waitcnt lgkmcnt(3)
	v_mfma_f32_16x16x32_bf16 v[84:87], v[140:143], v[160:163], v[84:87]
	ds_read_b128 v[160:163], v115 offset:17408
	s_waitcnt lgkmcnt(3)
	v_mfma_f32_16x16x32_bf16 v[80:83], v[140:143], v[164:167], v[80:83]
	ds_read_b128 v[164:167], v115 offset:18432
	s_waitcnt lgkmcnt(3)
	v_mfma_f32_16x16x32_bf16 v[76:79], v[140:143], v[132:135], v[76:79]
	ds_read_b128 v[132:135], v115 offset:19456
	s_waitcnt lgkmcnt(3)
	s_cmp_lg_u32 s63, 0
	s_cbranch_scc1 .Lmain_skip1
	s_or_b32 s62, s61, 0x800
	s_mov_b32 m0, s48
	s_nop 0
	buffer_load_dwordx4 v113, s[12:15], s62 offen nt lds
.Lmain_skip1:
	v_mfma_f32_16x16x32_bf16 v[148:151], v[144:147], v[156:159], v[148:151]
	ds_read_b128 v[156:159], v115 offset:20480
	s_waitcnt lgkmcnt(3)
	v_mfma_f32_16x16x32_bf16 v[152:155], v[144:147], v[160:163], v[152:155]
	ds_read_b128 v[160:163], v115 offset:21504
	s_waitcnt lgkmcnt(3)
	v_mfma_f32_16x16x32_bf16 v[96:99], v[144:147], v[164:167], v[96:99]
	ds_read_b128 v[164:167], v115 offset:22528
	s_waitcnt lgkmcnt(3)
	v_mfma_f32_16x16x32_bf16 v[92:95], v[144:147], v[132:135], v[92:95]
	ds_read_b128 v[132:135], v115 offset:23552
	s_waitcnt lgkmcnt(3)
	v_mfma_f32_16x16x32_bf16 v[88:91], v[144:147], v[156:159], v[88:91]
	ds_read_b128 v[156:159], v115 offset:24576
	s_waitcnt lgkmcnt(3)
	v_mfma_f32_16x16x32_bf16 v[84:87], v[144:147], v[160:163], v[84:87]
	ds_read_b128 v[160:163], v115 offset:25600
	s_waitcnt lgkmcnt(3)
	v_mfma_f32_16x16x32_bf16 v[80:83], v[144:147], v[164:167], v[80:83]
	ds_read_b128 v[164:167], v115 offset:26624
	s_waitcnt lgkmcnt(3)
	v_mfma_f32_16x16x32_bf16 v[76:79], v[144:147], v[132:135], v[76:79]
	ds_read_b128 v[132:135], v115 offset:27648
	s_waitcnt lgkmcnt(3)
	v_mfma_f32_16x16x32_bf16 v[148:151], v[128:131], v[156:159], v[148:151]
	ds_read_b128 v[156:159], v115 offset:28672
	s_waitcnt lgkmcnt(3)
	v_mfma_f32_16x16x32_bf16 v[152:155], v[128:131], v[160:163], v[152:155]
	ds_read_b128 v[160:163], v115 offset:29696
	s_waitcnt lgkmcnt(3)
	v_mfma_f32_16x16x32_bf16 v[96:99], v[128:131], v[164:167], v[96:99]
	ds_read_b128 v[164:167], v115 offset:30720
	s_waitcnt lgkmcnt(3)
	v_mfma_f32_16x16x32_bf16 v[92:95], v[128:131], v[132:135], v[92:95]
	ds_read_b128 v[132:135], v115 offset:31744
	s_waitcnt lgkmcnt(3)
	v_mfma_f32_16x16x32_bf16 v[88:91], v[128:131], v[156:159], v[88:91]
	s_waitcnt lgkmcnt(2)
	v_mfma_f32_16x16x32_bf16 v[84:87], v[128:131], v[160:163], v[84:87]
	s_waitcnt lgkmcnt(1)
	v_mfma_f32_16x16x32_bf16 v[80:83], v[128:131], v[164:167], v[80:83]
	s_waitcnt lgkmcnt(0)
	v_mfma_f32_16x16x32_bf16 v[76:79], v[128:131], v[132:135], v[76:79]
	ds_read2_b32 v[136:137], v114 offset0:128 offset1:144
	ds_read2_b32 v[138:139], v125 offset1:16
	ds_read2_b32 v[140:141], v114 offset0:160 offset1:176
	ds_read2_b32 v[142:143], v125 offset0:32 offset1:48
	ds_read2_b32 v[144:145], v114 offset0:192 offset1:208
	ds_read2_b32 v[146:147], v125 offset0:64 offset1:80
	ds_read2_b32 v[156:157], v114 offset0:224 offset1:240
	ds_read2_b32 v[158:159], v125 offset0:96 offset1:112
	v_fma_f32 v70, v149, v149, 0
	v_fmac_f32_e32 v70, v153, v153
	v_fmac_f32_e32 v70, v97, v97
	v_fmac_f32_e32 v70, v93, v93
	v_fmac_f32_e32 v70, v89, v89
	v_fmac_f32_e32 v70, v85, v85
	v_fmac_f32_e32 v70, v81, v81
	v_fmac_f32_e32 v70, v77, v77
	v_fma_f32 v68, v148, v148, 0
	v_fmac_f32_e32 v68, v152, v152
	v_add_f32_dpp v70, v70, v70 quad_perm:[1,0,3,2] row_mask:0xf bank_mask:0xf bound_ctrl:1
	v_fmac_f32_e32 v68, v96, v96
	v_fmac_f32_e32 v68, v92, v92
	v_add_f32_dpp v70, v70, v70 quad_perm:[2,3,0,1] row_mask:0xf bank_mask:0xf bound_ctrl:1
	v_fmac_f32_e32 v68, v88, v88
	v_fmac_f32_e32 v68, v84, v84
	v_add_f32_dpp v70, v70, v70 row_half_mirror row_mask:0xf bank_mask:0xf bound_ctrl:1
	v_fmac_f32_e32 v68, v80, v80
	v_fmac_f32_e32 v68, v76, v76
	v_add_f32_dpp v70, v70, v70 row_mirror row_mask:0xf bank_mask:0xf bound_ctrl:1
	v_fmamk_f32 v70, v70, 0x3c000000, v124
	s_cmp_lg_u32 s63, 0
	s_cbranch_scc1 .Lmain_skip2
	s_or_b32 s62, s61, 0x1000
	s_mov_b32 m0, s49
	s_nop 0
	buffer_load_dwordx4 v113, s[12:15], s62 offen nt lds
